# baseline (speedup 1.0000x reference)
_Z11align_fusedPKfS0_PKiPf:
	s_cmp_ge_u32 s2, 1024
	s_cbranch_scc1 .Lexit
	s_load_dwordx8 s[4:11], s[0:1], 0x0
	s_and_b32 s3, s2, 7
	s_lshl_b32 s3, s3, 10
	s_lshr_b32 s2, s2, 3
	s_add_i32 s2, s3, s2
	s_mul_i32 s12, s2, 0x5dc0
	v_and_b32_e32 v7, 63, v0
	v_readfirstlane_b32 s13, v0
	v_lshlrev_b32_e32 v1, 4, v7
	v_mul_u32_u24_e32 v3, 12, v7
	s_mul_i32 s18, s13, 96
	s_mul_i32 s3, s13, 6
	s_sub_u32 s3, 0x49c, s3
	v_cmp_gt_u32_e64 s[14:15], s3, v7
	v_add_u32_e32 v2, s18, v1
	v_add_u32_e32 v3, s18, v3
	v_add_u32_e32 v4, 0x600, v3
	v_add_u32_e32 v67, 0xc00, v3
	v_add_u32_e32 v68, 0x1200, v3
	s_add_u32 s12, s12, s18
	s_add_u32 s12, s12, 0x800
	s_mov_b32 s39, 0x2ee000
	s_mov_b32 s38, 8
	s_mov_b32 s36, 0
	s_mov_b32 s37, 0xf0000
	s_waitcnt lgkmcnt(0)
	s_add_u32 s4, s4, s12
	s_addc_u32 s5, s5, 0
	s_add_u32 s10, s10, s12
	s_addc_u32 s11, s11, 0
	s_cmp_lg_u32 s13, 0
	s_cbranch_scc1 .Lfirst_loads
	v_lshlrev_b32_e32 v5, 2, v7
	global_load_dword v5, v5, s[8:9]
	global_load_dwordx3 v[64:66], v3, s[6:7] nt
	s_mov_b32 s20, 0
	s_mov_b32 s21, 0x10000
	s_mov_b32 s22, 0
	s_mov_b32 s23, 0x20000
	s_mov_b32 s24, 0
	s_mov_b32 s25, 0x40000
	s_mov_b32 s26, 0
	s_mov_b32 s27, 0x80000
	s_waitcnt vmcnt(0)
	v_mul_u32_u24_e32 v5, 12, v5
	v_add_f32_dpp v52, v64, v64 quad_perm:[1,0,3,2] row_mask:0xf bank_mask:0xf
	v_add_f32_dpp v53, v65, v65 quad_perm:[1,0,3,2] row_mask:0xf bank_mask:0xf
	v_add_f32_dpp v54, v66, v66 quad_perm:[1,0,3,2] row_mask:0xf bank_mask:0xf
	v_add_f32_dpp v52, v52, v52 quad_perm:[2,3,0,1] row_mask:0xf bank_mask:0xf
	v_add_f32_dpp v53, v53, v53 quad_perm:[2,3,0,1] row_mask:0xf bank_mask:0xf
	v_add_f32_dpp v54, v54, v54 quad_perm:[2,3,0,1] row_mask:0xf bank_mask:0xf
	v_add_f32_dpp v52, v52, v52 row_half_mirror row_mask:0xf bank_mask:0xf
	v_add_f32_dpp v53, v53, v53 row_half_mirror row_mask:0xf bank_mask:0xf
	v_add_f32_dpp v54, v54, v54 row_half_mirror row_mask:0xf bank_mask:0xf
	v_add_f32_dpp v52, v52, v52 row_mirror row_mask:0xf bank_mask:0xf
	v_add_f32_dpp v53, v53, v53 row_mirror row_mask:0xf bank_mask:0xf
	v_add_f32_dpp v54, v54, v54 row_mirror row_mask:0xf bank_mask:0xf
	v_add_f32_dpp v52, v52, v52 row_bcast:15 row_mask:0xa bank_mask:0xf
	v_add_f32_dpp v53, v53, v53 row_bcast:15 row_mask:0xa bank_mask:0xf
	v_add_f32_dpp v54, v54, v54 row_bcast:15 row_mask:0xa bank_mask:0xf
	v_add_f32_dpp v52, v52, v52 row_bcast:31 row_mask:0xc bank_mask:0xf
	v_add_f32_dpp v53, v53, v53 row_bcast:31 row_mask:0xc bank_mask:0xf
	v_add_f32_dpp v54, v54, v54 row_bcast:31 row_mask:0xc bank_mask:0xf
	v_readlane_b32 s28, v52, 63
	v_readlane_b32 s29, v53, 63
	v_readlane_b32 s30, v54, 63
	v_mov_b32_e32 v52, s28
	v_mov_b32_e32 v53, s29
	v_mov_b32_e32 v54, s30
	v_fmac_f32_e32 v64, 0xbc800000, v52
	v_fmac_f32_e32 v65, 0xbc800000, v53
	v_fmac_f32_e32 v66, 0xbc800000, v54
.Lfirst_loads:
	global_load_dwordx4 v[8:11], v1, s[4:5] offset:-2048 nt
	global_load_dwordx4 v[12:15], v1, s[4:5] offset:-1024 nt
	global_load_dwordx4 v[16:19], v1, s[4:5] offset:0 nt
	global_load_dwordx4 v[20:23], v1, s[4:5] offset:1024 nt
	global_load_dwordx4 v[24:27], v1, s[4:5] offset:2048 nt
	s_and_saveexec_b64 s[16:17], s[14:15]
	global_load_dwordx4 v[28:31], v1, s[4:5] offset:3072 nt
	s_mov_b64 exec, s[16:17]
	s_add_u32 s4, s4, s39
	s_addc_u32 s5, s5, 0
	s_waitcnt vmcnt(0)
.Lrow_loop:
	s_waitcnt vmcnt(6)
	ds_write_b128 v2, v[8:11]
	ds_write_b128 v2, v[12:15] offset:1024
	ds_write_b128 v2, v[16:19] offset:2048
	ds_write_b128 v2, v[20:23] offset:3072
	ds_write_b128 v2, v[24:27] offset:4096
	ds_write_b128 v2, v[28:31] offset:5120
	s_cmp_eq_u32 s38, 1
	s_cbranch_scc1 .Lno_prefetch
	global_load_dwordx4 v[8:11], v1, s[4:5] offset:-2048 nt
	global_load_dwordx4 v[12:15], v1, s[4:5] offset:-1024 nt
	global_load_dwordx4 v[16:19], v1, s[4:5] offset:0 nt
	global_load_dwordx4 v[20:23], v1, s[4:5] offset:1024 nt
	global_load_dwordx4 v[24:27], v1, s[4:5] offset:2048 nt
	s_and_saveexec_b64 s[16:17], s[14:15]
	global_load_dwordx4 v[28:31], v1, s[4:5] offset:3072 nt
	s_mov_b64 exec, s[16:17]
	s_add_u32 s4, s4, s39
	s_addc_u32 s5, s5, 0
.Lno_prefetch:
	s_waitcnt lgkmcnt(0)
	s_barrier
	s_cmp_lg_u32 s13, 0
	s_cbranch_scc1 .Lsolved
	ds_read_b32 v48, v5
	ds_read_b32 v49, v5 offset:4
	ds_read_b32 v50, v5 offset:8
	s_waitcnt lgkmcnt(0)
	v_add_f32_dpp v52, v48, v48 quad_perm:[1,0,3,2] row_mask:0xf bank_mask:0xf
	v_add_f32_dpp v53, v49, v49 quad_perm:[1,0,3,2] row_mask:0xf bank_mask:0xf
	v_add_f32_dpp v54, v50, v50 quad_perm:[1,0,3,2] row_mask:0xf bank_mask:0xf
	v_add_f32_dpp v52, v52, v52 quad_perm:[2,3,0,1] row_mask:0xf bank_mask:0xf
	v_add_f32_dpp v53, v53, v53 quad_perm:[2,3,0,1] row_mask:0xf bank_mask:0xf
	v_add_f32_dpp v54, v54, v54 quad_perm:[2,3,0,1] row_mask:0xf bank_mask:0xf
	v_add_f32_dpp v52, v52, v52 row_half_mirror row_mask:0xf bank_mask:0xf
	v_add_f32_dpp v53, v53, v53 row_half_mirror row_mask:0xf bank_mask:0xf
	v_add_f32_dpp v54, v54, v54 row_half_mirror row_mask:0xf bank_mask:0xf
	v_add_f32_dpp v52, v52, v52 row_mirror row_mask:0xf bank_mask:0xf
	v_add_f32_dpp v53, v53, v53 row_mirror row_mask:0xf bank_mask:0xf
	v_add_f32_dpp v54, v54, v54 row_mirror row_mask:0xf bank_mask:0xf
	v_add_f32_dpp v52, v52, v52 row_bcast:15 row_mask:0xa bank_mask:0xf
	v_add_f32_dpp v53, v53, v53 row_bcast:15 row_mask:0xa bank_mask:0xf
	v_add_f32_dpp v54, v54, v54 row_bcast:15 row_mask:0xa bank_mask:0xf
	v_add_f32_dpp v52, v52, v52 row_bcast:31 row_mask:0xc bank_mask:0xf
	v_add_f32_dpp v53, v53, v53 row_bcast:31 row_mask:0xc bank_mask:0xf
	v_add_f32_dpp v54, v54, v54 row_bcast:31 row_mask:0xc bank_mask:0xf
	v_readlane_b32 s32, v52, 63
	v_readlane_b32 s33, v53, 63
	v_readlane_b32 s34, v54, 63
	v_mov_b32_e32 v52, s32
	v_mov_b32_e32 v53, s33
	v_mov_b32_e32 v54, s34
	v_fmac_f32_e32 v48, 0xbc800000, v52
	v_fmac_f32_e32 v49, 0xbc800000, v53
	v_fmac_f32_e32 v50, 0xbc800000, v54
	v_mul_f32_e32 v52, v48, v64
	v_mul_f32_e32 v53, v48, v65
	v_mul_f32_e32 v54, v48, v66
	v_mul_f32_e32 v55, v49, v64
	v_mul_f32_e32 v56, v49, v65
	v_mul_f32_e32 v57, v49, v66
	v_mul_f32_e32 v58, v50, v64
	v_mul_f32_e32 v59, v50, v65
	v_mul_f32_e32 v60, v50, v66
	v_add_f32_dpp v52, v52, v52 quad_perm:[1,0,3,2] row_mask:0xf bank_mask:0xf
	v_add_f32_dpp v53, v53, v53 quad_perm:[1,0,3,2] row_mask:0xf bank_mask:0xf
	v_add_f32_dpp v54, v54, v54 quad_perm:[1,0,3,2] row_mask:0xf bank_mask:0xf
	v_add_f32_dpp v55, v55, v55 quad_perm:[1,0,3,2] row_mask:0xf bank_mask:0xf
	v_add_f32_dpp v56, v56, v56 quad_perm:[1,0,3,2] row_mask:0xf bank_mask:0xf
	v_add_f32_dpp v57, v57, v57 quad_perm:[1,0,3,2] row_mask:0xf bank_mask:0xf
	v_add_f32_dpp v58, v58, v58 quad_perm:[1,0,3,2] row_mask:0xf bank_mask:0xf
	v_add_f32_dpp v59, v59, v59 quad_perm:[1,0,3,2] row_mask:0xf bank_mask:0xf
	v_add_f32_dpp v60, v60, v60 quad_perm:[1,0,3,2] row_mask:0xf bank_mask:0xf
	v_add_f32_dpp v52, v52, v52 quad_perm:[2,3,0,1] row_mask:0xf bank_mask:0xf
	v_add_f32_dpp v53, v53, v53 quad_perm:[2,3,0,1] row_mask:0xf bank_mask:0xf
	v_add_f32_dpp v54, v54, v54 quad_perm:[2,3,0,1] row_mask:0xf bank_mask:0xf
	v_add_f32_dpp v55, v55, v55 quad_perm:[2,3,0,1] row_mask:0xf bank_mask:0xf
	v_add_f32_dpp v56, v56, v56 quad_perm:[2,3,0,1] row_mask:0xf bank_mask:0xf
	v_add_f32_dpp v57, v57, v57 quad_perm:[2,3,0,1] row_mask:0xf bank_mask:0xf
	v_add_f32_dpp v58, v58, v58 quad_perm:[2,3,0,1] row_mask:0xf bank_mask:0xf
	v_add_f32_dpp v59, v59, v59 quad_perm:[2,3,0,1] row_mask:0xf bank_mask:0xf
	v_add_f32_dpp v60, v60, v60 quad_perm:[2,3,0,1] row_mask:0xf bank_mask:0xf
	v_add_f32_dpp v52, v52, v52 row_half_mirror row_mask:0xf bank_mask:0xf
	v_add_f32_dpp v53, v53, v53 row_half_mirror row_mask:0xf bank_mask:0xf
	v_add_f32_dpp v54, v54, v54 row_half_mirror row_mask:0xf bank_mask:0xf
	v_add_f32_dpp v55, v55, v55 row_half_mirror row_mask:0xf bank_mask:0xf
	v_add_f32_dpp v56, v56, v56 row_half_mirror row_mask:0xf bank_mask:0xf
	v_add_f32_dpp v57, v57, v57 row_half_mirror row_mask:0xf bank_mask:0xf
	v_add_f32_dpp v58, v58, v58 row_half_mirror row_mask:0xf bank_mask:0xf
	v_add_f32_dpp v59, v59, v59 row_half_mirror row_mask:0xf bank_mask:0xf
	v_add_f32_dpp v60, v60, v60 row_half_mirror row_mask:0xf bank_mask:0xf
	v_add_f32_dpp v52, v52, v52 row_mirror row_mask:0xf bank_mask:0xf
	v_add_f32_dpp v53, v53, v53 row_mirror row_mask:0xf bank_mask:0xf
	v_add_f32_dpp v54, v54, v54 row_mirror row_mask:0xf bank_mask:0xf
	v_add_f32_dpp v55, v55, v55 row_mirror row_mask:0xf bank_mask:0xf
	v_add_f32_dpp v56, v56, v56 row_mirror row_mask:0xf bank_mask:0xf
	v_add_f32_dpp v57, v57, v57 row_mirror row_mask:0xf bank_mask:0xf
	v_add_f32_dpp v58, v58, v58 row_mirror row_mask:0xf bank_mask:0xf
	v_add_f32_dpp v59, v59, v59 row_mirror row_mask:0xf bank_mask:0xf
	v_add_f32_dpp v60, v60, v60 row_mirror row_mask:0xf bank_mask:0xf
	v_add_f32_dpp v52, v52, v52 row_bcast:15 row_mask:0xa bank_mask:0xf
	v_add_f32_dpp v53, v53, v53 row_bcast:15 row_mask:0xa bank_mask:0xf
	v_add_f32_dpp v54, v54, v54 row_bcast:15 row_mask:0xa bank_mask:0xf
	v_add_f32_dpp v55, v55, v55 row_bcast:15 row_mask:0xa bank_mask:0xf
	v_add_f32_dpp v56, v56, v56 row_bcast:15 row_mask:0xa bank_mask:0xf
	v_add_f32_dpp v57, v57, v57 row_bcast:15 row_mask:0xa bank_mask:0xf
	v_add_f32_dpp v58, v58, v58 row_bcast:15 row_mask:0xa bank_mask:0xf
	v_add_f32_dpp v59, v59, v59 row_bcast:15 row_mask:0xa bank_mask:0xf
	v_add_f32_dpp v60, v60, v60 row_bcast:15 row_mask:0xa bank_mask:0xf
	v_add_f32_dpp v52, v52, v52 row_bcast:31 row_mask:0xc bank_mask:0xf
	v_add_f32_dpp v53, v53, v53 row_bcast:31 row_mask:0xc bank_mask:0xf
	v_add_f32_dpp v54, v54, v54 row_bcast:31 row_mask:0xc bank_mask:0xf
	v_add_f32_dpp v55, v55, v55 row_bcast:31 row_mask:0xc bank_mask:0xf
	v_add_f32_dpp v56, v56, v56 row_bcast:31 row_mask:0xc bank_mask:0xf
	v_add_f32_dpp v57, v57, v57 row_bcast:31 row_mask:0xc bank_mask:0xf
	v_add_f32_dpp v58, v58, v58 row_bcast:31 row_mask:0xc bank_mask:0xf
	v_add_f32_dpp v59, v59, v59 row_bcast:31 row_mask:0xc bank_mask:0xf
	v_add_f32_dpp v60, v60, v60 row_bcast:31 row_mask:0xc bank_mask:0xf
	v_cndmask_b32_e64 v52, v52, v55, s[22:23]
	v_cndmask_b32_e64 v53, v53, v56, s[22:23]
	v_cndmask_b32_e64 v54, v54, v57, s[22:23]
	v_cndmask_b32_e64 v52, v52, v58, s[24:25]
	v_cndmask_b32_e64 v53, v53, v59, s[24:25]
	v_cndmask_b32_e64 v54, v54, v60, s[24:25]
	v_cndmask_b32_e64 v52, v52, 0, s[26:27]
	v_cndmask_b32_e64 v53, v53, 0, s[26:27]
	v_cndmask_b32_e64 v54, v54, 0, s[26:27]
	v_cndmask_b32_e64 v40, 0, 1.0, s[20:21]
	v_cndmask_b32_e64 v41, 0, 1.0, s[22:23]
	v_cndmask_b32_e64 v42, 0, 1.0, s[24:25]
	v_mul_f32_e32 v55, v52, v52
	v_mul_f32_e32 v56, v53, v53
	v_mul_f32_e32 v57, v52, v53
	v_add_f32_dpp v55, v55, v55 quad_perm:[1,0,3,2] row_mask:0xf bank_mask:0xf
	v_add_f32_dpp v56, v56, v56 quad_perm:[1,0,3,2] row_mask:0xf bank_mask:0xf
	v_add_f32_dpp v57, v57, v57 quad_perm:[1,0,3,2] row_mask:0xf bank_mask:0xf
	v_add_f32_dpp v55, v55, v55 quad_perm:[2,3,0,1] row_mask:0xf bank_mask:0xf
	v_add_f32_dpp v56, v56, v56 quad_perm:[2,3,0,1] row_mask:0xf bank_mask:0xf
	v_add_f32_dpp v57, v57, v57 quad_perm:[2,3,0,1] row_mask:0xf bank_mask:0xf
	v_sub_f32_e32 v60, v56, v55
	v_mul_f32_e32 v58, v57, v57
	v_cmp_gt_f32_e32 vcc, 0, v60
	v_mul_f32_e32 v59, v60, v60
	v_fmac_f32_e32 v59, 4.0, v58
	v_sqrt_f32_e32 v59, v59
	s_nop 0
	v_add_f32_e64 v59, |v60|, v59
	v_add_f32_e32 v59, 0x0da24260, v59
	v_rcp_f32_e32 v59, v59
	v_add_f32_e32 v58, v57, v57
	v_mul_f32_e32 v59, v58, v59
	v_cndmask_b32_e64 v59, v59, -v59, vcc
	v_fma_f32 v58, v59, v59, 1.0
	v_rsq_f32_e32 v61, v58
	s_nop 0
	v_mul_f32_e32 v62, v61, v59
	v_mul_f32_e32 v55, v62, v53
	v_mul_f32_e32 v56, v62, v52
	v_fma_f32 v52, v61, v52, -v55
	v_fma_f32 v53, v61, v53, v56
	v_mul_f32_e32 v55, v52, v52
	v_mul_f32_e32 v56, v54, v54
	v_mul_f32_e32 v57, v52, v54
	v_add_f32_dpp v55, v55, v55 quad_perm:[1,0,3,2] row_mask:0xf bank_mask:0xf
	v_add_f32_dpp v56, v56, v56 quad_perm:[1,0,3,2] row_mask:0xf bank_mask:0xf
	v_add_f32_dpp v57, v57, v57 quad_perm:[1,0,3,2] row_mask:0xf bank_mask:0xf
	v_add_f32_dpp v55, v55, v55 quad_perm:[2,3,0,1] row_mask:0xf bank_mask:0xf
	v_add_f32_dpp v56, v56, v56 quad_perm:[2,3,0,1] row_mask:0xf bank_mask:0xf
	v_add_f32_dpp v57, v57, v57 quad_perm:[2,3,0,1] row_mask:0xf bank_mask:0xf
	v_sub_f32_e32 v60, v56, v55
	v_mul_f32_e32 v58, v57, v57
	v_cmp_gt_f32_e32 vcc, 0, v60
	v_mul_f32_e32 v59, v60, v60
	v_fmac_f32_e32 v59, 4.0, v58
	v_sqrt_f32_e32 v59, v59
	v_mul_f32_e32 v63, v62, v41
	v_mul_f32_e32 v43, v62, v40
	v_fma_f32 v40, v61, v40, -v63
	v_fma_f32 v41, v61, v41, v43
	v_add_f32_e64 v59, |v60|, v59
	v_add_f32_e32 v59, 0x0da24260, v59
	v_rcp_f32_e32 v59, v59
	v_add_f32_e32 v58, v57, v57
	v_mul_f32_e32 v59, v58, v59
	v_cndmask_b32_e64 v59, v59, -v59, vcc
	v_fma_f32 v58, v59, v59, 1.0
	v_rsq_f32_e32 v61, v58
	s_nop 0
	v_mul_f32_e32 v62, v61, v59
	v_mul_f32_e32 v55, v62, v54
	v_mul_f32_e32 v56, v62, v52
	v_fma_f32 v52, v61, v52, -v55
	v_fma_f32 v54, v61, v54, v56
	v_mul_f32_e32 v55, v53, v53
	v_mul_f32_e32 v56, v54, v54
	v_mul_f32_e32 v57, v53, v54
	v_add_f32_dpp v55, v55, v55 quad_perm:[1,0,3,2] row_mask:0xf bank_mask:0xf
	v_add_f32_dpp v56, v56, v56 quad_perm:[1,0,3,2] row_mask:0xf bank_mask:0xf
	v_add_f32_dpp v57, v57, v57 quad_perm:[1,0,3,2] row_mask:0xf bank_mask:0xf
	v_add_f32_dpp v55, v55, v55 quad_perm:[2,3,0,1] row_mask:0xf bank_mask:0xf
	v_add_f32_dpp v56, v56, v56 quad_perm:[2,3,0,1] row_mask:0xf bank_mask:0xf
	v_add_f32_dpp v57, v57, v57 quad_perm:[2,3,0,1] row_mask:0xf bank_mask:0xf
	v_sub_f32_e32 v60, v56, v55
	v_mul_f32_e32 v58, v57, v57
	v_cmp_gt_f32_e32 vcc, 0, v60
	v_mul_f32_e32 v59, v60, v60
	v_fmac_f32_e32 v59, 4.0, v58
	v_sqrt_f32_e32 v59, v59
	v_mul_f32_e32 v63, v62, v42
	v_mul_f32_e32 v43, v62, v40
	v_fma_f32 v40, v61, v40, -v63
	v_fma_f32 v42, v61, v42, v43
	v_add_f32_e64 v59, |v60|, v59
	v_add_f32_e32 v59, 0x0da24260, v59
	v_rcp_f32_e32 v59, v59
	v_add_f32_e32 v58, v57, v57
	v_mul_f32_e32 v59, v58, v59
	v_cndmask_b32_e64 v59, v59, -v59, vcc
	v_fma_f32 v58, v59, v59, 1.0
	v_rsq_f32_e32 v61, v58
	s_nop 0
	v_mul_f32_e32 v62, v61, v59
	v_mul_f32_e32 v55, v62, v54
	v_mul_f32_e32 v56, v62, v53
	v_fma_f32 v53, v61, v53, -v55
	v_fma_f32 v54, v61, v54, v56
	v_mul_f32_e32 v55, v52, v52
	v_mul_f32_e32 v56, v53, v53
	v_mul_f32_e32 v57, v52, v53
	v_add_f32_dpp v55, v55, v55 quad_perm:[1,0,3,2] row_mask:0xf bank_mask:0xf
	v_add_f32_dpp v56, v56, v56 quad_perm:[1,0,3,2] row_mask:0xf bank_mask:0xf
	v_add_f32_dpp v57, v57, v57 quad_perm:[1,0,3,2] row_mask:0xf bank_mask:0xf
	v_add_f32_dpp v55, v55, v55 quad_perm:[2,3,0,1] row_mask:0xf bank_mask:0xf
	v_add_f32_dpp v56, v56, v56 quad_perm:[2,3,0,1] row_mask:0xf bank_mask:0xf
	v_add_f32_dpp v57, v57, v57 quad_perm:[2,3,0,1] row_mask:0xf bank_mask:0xf
	v_sub_f32_e32 v60, v56, v55
	v_mul_f32_e32 v58, v57, v57
	v_cmp_gt_f32_e32 vcc, 0, v60
	v_mul_f32_e32 v59, v60, v60
	v_fmac_f32_e32 v59, 4.0, v58
	v_sqrt_f32_e32 v59, v59
	v_mul_f32_e32 v63, v62, v42
	v_mul_f32_e32 v43, v62, v41
	v_fma_f32 v41, v61, v41, -v63
	v_fma_f32 v42, v61, v42, v43
	v_add_f32_e64 v59, |v60|, v59
	v_add_f32_e32 v59, 0x0da24260, v59
	v_rcp_f32_e32 v59, v59
	v_add_f32_e32 v58, v57, v57
	v_mul_f32_e32 v59, v58, v59
	v_cndmask_b32_e64 v59, v59, -v59, vcc
	v_fma_f32 v58, v59, v59, 1.0
	v_rsq_f32_e32 v61, v58
	s_nop 0
	v_mul_f32_e32 v62, v61, v59
	v_mul_f32_e32 v55, v62, v53
	v_mul_f32_e32 v56, v62, v52
	v_fma_f32 v52, v61, v52, -v55
	v_fma_f32 v53, v61, v53, v56
	v_mul_f32_e32 v55, v52, v52
	v_mul_f32_e32 v56, v54, v54
	v_mul_f32_e32 v57, v52, v54
	v_add_f32_dpp v55, v55, v55 quad_perm:[1,0,3,2] row_mask:0xf bank_mask:0xf
	v_add_f32_dpp v56, v56, v56 quad_perm:[1,0,3,2] row_mask:0xf bank_mask:0xf
	v_add_f32_dpp v57, v57, v57 quad_perm:[1,0,3,2] row_mask:0xf bank_mask:0xf
	v_add_f32_dpp v55, v55, v55 quad_perm:[2,3,0,1] row_mask:0xf bank_mask:0xf
	v_add_f32_dpp v56, v56, v56 quad_perm:[2,3,0,1] row_mask:0xf bank_mask:0xf
	v_add_f32_dpp v57, v57, v57 quad_perm:[2,3,0,1] row_mask:0xf bank_mask:0xf
	v_sub_f32_e32 v60, v56, v55
	v_mul_f32_e32 v58, v57, v57
	v_cmp_gt_f32_e32 vcc, 0, v60
	v_mul_f32_e32 v59, v60, v60
	v_fmac_f32_e32 v59, 4.0, v58
	v_sqrt_f32_e32 v59, v59
	v_mul_f32_e32 v63, v62, v41
	v_mul_f32_e32 v43, v62, v40
	v_fma_f32 v40, v61, v40, -v63
	v_fma_f32 v41, v61, v41, v43
	v_add_f32_e64 v59, |v60|, v59
	v_add_f32_e32 v59, 0x0da24260, v59
	v_rcp_f32_e32 v59, v59
	v_add_f32_e32 v58, v57, v57
	v_mul_f32_e32 v59, v58, v59
	v_cndmask_b32_e64 v59, v59, -v59, vcc
	v_fma_f32 v58, v59, v59, 1.0
	v_rsq_f32_e32 v61, v58
	s_nop 0
	v_mul_f32_e32 v62, v61, v59
	v_mul_f32_e32 v55, v62, v54
	v_mul_f32_e32 v56, v62, v52
	v_fma_f32 v52, v61, v52, -v55
	v_fma_f32 v54, v61, v54, v56
	v_mul_f32_e32 v55, v53, v53
	v_mul_f32_e32 v56, v54, v54
	v_mul_f32_e32 v57, v53, v54
	v_add_f32_dpp v55, v55, v55 quad_perm:[1,0,3,2] row_mask:0xf bank_mask:0xf
	v_add_f32_dpp v56, v56, v56 quad_perm:[1,0,3,2] row_mask:0xf bank_mask:0xf
	v_add_f32_dpp v57, v57, v57 quad_perm:[1,0,3,2] row_mask:0xf bank_mask:0xf
	v_add_f32_dpp v55, v55, v55 quad_perm:[2,3,0,1] row_mask:0xf bank_mask:0xf
	v_add_f32_dpp v56, v56, v56 quad_perm:[2,3,0,1] row_mask:0xf bank_mask:0xf
	v_add_f32_dpp v57, v57, v57 quad_perm:[2,3,0,1] row_mask:0xf bank_mask:0xf
	v_sub_f32_e32 v60, v56, v55
	v_mul_f32_e32 v58, v57, v57
	v_cmp_gt_f32_e32 vcc, 0, v60
	v_mul_f32_e32 v59, v60, v60
	v_fmac_f32_e32 v59, 4.0, v58
	v_sqrt_f32_e32 v59, v59
	v_mul_f32_e32 v63, v62, v42
	v_mul_f32_e32 v43, v62, v40
	v_fma_f32 v40, v61, v40, -v63
	v_fma_f32 v42, v61, v42, v43
	v_add_f32_e64 v59, |v60|, v59
	v_add_f32_e32 v59, 0x0da24260, v59
	v_rcp_f32_e32 v59, v59
	v_add_f32_e32 v58, v57, v57
	v_mul_f32_e32 v59, v58, v59
	v_cndmask_b32_e64 v59, v59, -v59, vcc
	v_fma_f32 v58, v59, v59, 1.0
	v_rsq_f32_e32 v61, v58
	s_nop 0
	v_mul_f32_e32 v62, v61, v59
	v_mul_f32_e32 v55, v62, v54
	v_mul_f32_e32 v56, v62, v53
	v_fma_f32 v53, v61, v53, -v55
	v_fma_f32 v54, v61, v54, v56
	v_mul_f32_e32 v55, v52, v52
	v_mul_f32_e32 v56, v53, v53
	v_mul_f32_e32 v57, v52, v53
	v_add_f32_dpp v55, v55, v55 quad_perm:[1,0,3,2] row_mask:0xf bank_mask:0xf
	v_add_f32_dpp v56, v56, v56 quad_perm:[1,0,3,2] row_mask:0xf bank_mask:0xf
	v_add_f32_dpp v57, v57, v57 quad_perm:[1,0,3,2] row_mask:0xf bank_mask:0xf
	v_add_f32_dpp v55, v55, v55 quad_perm:[2,3,0,1] row_mask:0xf bank_mask:0xf
	v_add_f32_dpp v56, v56, v56 quad_perm:[2,3,0,1] row_mask:0xf bank_mask:0xf
	v_add_f32_dpp v57, v57, v57 quad_perm:[2,3,0,1] row_mask:0xf bank_mask:0xf
	v_sub_f32_e32 v60, v56, v55
	v_mul_f32_e32 v58, v57, v57
	v_cmp_gt_f32_e32 vcc, 0, v60
	v_mul_f32_e32 v59, v60, v60
	v_fmac_f32_e32 v59, 4.0, v58
	v_sqrt_f32_e32 v59, v59
	v_mul_f32_e32 v63, v62, v42
	v_mul_f32_e32 v43, v62, v41
	v_fma_f32 v41, v61, v41, -v63
	v_fma_f32 v42, v61, v42, v43
	v_add_f32_e64 v59, |v60|, v59
	v_add_f32_e32 v59, 0x0da24260, v59
	v_rcp_f32_e32 v59, v59
	v_add_f32_e32 v58, v57, v57
	v_mul_f32_e32 v59, v58, v59
	v_cndmask_b32_e64 v59, v59, -v59, vcc
	v_fma_f32 v58, v59, v59, 1.0
	v_rsq_f32_e32 v61, v58
	s_nop 0
	v_mul_f32_e32 v62, v61, v59
	v_mul_f32_e32 v55, v62, v53
	v_mul_f32_e32 v56, v62, v52
	v_fma_f32 v52, v61, v52, -v55
	v_fma_f32 v53, v61, v53, v56
	v_mul_f32_e32 v55, v52, v52
	v_mul_f32_e32 v56, v54, v54
	v_mul_f32_e32 v57, v52, v54
	v_add_f32_dpp v55, v55, v55 quad_perm:[1,0,3,2] row_mask:0xf bank_mask:0xf
	v_add_f32_dpp v56, v56, v56 quad_perm:[1,0,3,2] row_mask:0xf bank_mask:0xf
	v_add_f32_dpp v57, v57, v57 quad_perm:[1,0,3,2] row_mask:0xf bank_mask:0xf
	v_add_f32_dpp v55, v55, v55 quad_perm:[2,3,0,1] row_mask:0xf bank_mask:0xf
	v_add_f32_dpp v56, v56, v56 quad_perm:[2,3,0,1] row_mask:0xf bank_mask:0xf
	v_add_f32_dpp v57, v57, v57 quad_perm:[2,3,0,1] row_mask:0xf bank_mask:0xf
	v_sub_f32_e32 v60, v56, v55
	v_mul_f32_e32 v58, v57, v57
	v_cmp_gt_f32_e32 vcc, 0, v60
	v_mul_f32_e32 v59, v60, v60
	v_fmac_f32_e32 v59, 4.0, v58
	v_sqrt_f32_e32 v59, v59
	v_mul_f32_e32 v63, v62, v41
	v_mul_f32_e32 v43, v62, v40
	v_fma_f32 v40, v61, v40, -v63
	v_fma_f32 v41, v61, v41, v43
	v_add_f32_e64 v59, |v60|, v59
	v_add_f32_e32 v59, 0x0da24260, v59
	v_rcp_f32_e32 v59, v59
	v_add_f32_e32 v58, v57, v57
	v_mul_f32_e32 v59, v58, v59
	v_cndmask_b32_e64 v59, v59, -v59, vcc
	v_fma_f32 v58, v59, v59, 1.0
	v_rsq_f32_e32 v61, v58
	s_nop 0
	v_mul_f32_e32 v62, v61, v59
	v_mul_f32_e32 v55, v62, v54
	v_mul_f32_e32 v56, v62, v52
	v_fma_f32 v52, v61, v52, -v55
	v_fma_f32 v54, v61, v54, v56
	v_mul_f32_e32 v55, v53, v53
	v_mul_f32_e32 v56, v54, v54
	v_mul_f32_e32 v57, v53, v54
	v_add_f32_dpp v55, v55, v55 quad_perm:[1,0,3,2] row_mask:0xf bank_mask:0xf
	v_add_f32_dpp v56, v56, v56 quad_perm:[1,0,3,2] row_mask:0xf bank_mask:0xf
	v_add_f32_dpp v57, v57, v57 quad_perm:[1,0,3,2] row_mask:0xf bank_mask:0xf
	v_add_f32_dpp v55, v55, v55 quad_perm:[2,3,0,1] row_mask:0xf bank_mask:0xf
	v_add_f32_dpp v56, v56, v56 quad_perm:[2,3,0,1] row_mask:0xf bank_mask:0xf
	v_add_f32_dpp v57, v57, v57 quad_perm:[2,3,0,1] row_mask:0xf bank_mask:0xf
	v_sub_f32_e32 v60, v56, v55
	v_mul_f32_e32 v58, v57, v57
	v_cmp_gt_f32_e32 vcc, 0, v60
	v_mul_f32_e32 v59, v60, v60
	v_fmac_f32_e32 v59, 4.0, v58
	v_sqrt_f32_e32 v59, v59
	v_mul_f32_e32 v63, v62, v42
	v_mul_f32_e32 v43, v62, v40
	v_fma_f32 v40, v61, v40, -v63
	v_fma_f32 v42, v61, v42, v43
	v_add_f32_e64 v59, |v60|, v59
	v_add_f32_e32 v59, 0x0da24260, v59
	v_rcp_f32_e32 v59, v59
	v_add_f32_e32 v58, v57, v57
	v_mul_f32_e32 v59, v58, v59
	v_cndmask_b32_e64 v59, v59, -v59, vcc
	v_fma_f32 v58, v59, v59, 1.0
	v_rsq_f32_e32 v61, v58
	s_nop 0
	v_mul_f32_e32 v62, v61, v59
	v_mul_f32_e32 v55, v62, v54
	v_mul_f32_e32 v56, v62, v53
	v_fma_f32 v53, v61, v53, -v55
	v_fma_f32 v54, v61, v54, v56
	v_mul_f32_e32 v55, v52, v52
	v_mul_f32_e32 v56, v53, v53
	v_mul_f32_e32 v57, v52, v53
	v_add_f32_dpp v55, v55, v55 quad_perm:[1,0,3,2] row_mask:0xf bank_mask:0xf
	v_add_f32_dpp v56, v56, v56 quad_perm:[1,0,3,2] row_mask:0xf bank_mask:0xf
	v_add_f32_dpp v57, v57, v57 quad_perm:[1,0,3,2] row_mask:0xf bank_mask:0xf
	v_add_f32_dpp v55, v55, v55 quad_perm:[2,3,0,1] row_mask:0xf bank_mask:0xf
	v_add_f32_dpp v56, v56, v56 quad_perm:[2,3,0,1] row_mask:0xf bank_mask:0xf
	v_add_f32_dpp v57, v57, v57 quad_perm:[2,3,0,1] row_mask:0xf bank_mask:0xf
	v_sub_f32_e32 v60, v56, v55
	v_mul_f32_e32 v58, v57, v57
	v_cmp_gt_f32_e32 vcc, 0, v60
	v_mul_f32_e32 v59, v60, v60
	v_fmac_f32_e32 v59, 4.0, v58
	v_sqrt_f32_e32 v59, v59
	v_mul_f32_e32 v63, v62, v42
	v_mul_f32_e32 v43, v62, v41
	v_fma_f32 v41, v61, v41, -v63
	v_fma_f32 v42, v61, v42, v43
	v_add_f32_e64 v59, |v60|, v59
	v_add_f32_e32 v59, 0x0da24260, v59
	v_rcp_f32_e32 v59, v59
	v_add_f32_e32 v58, v57, v57
	v_mul_f32_e32 v59, v58, v59
	v_cndmask_b32_e64 v59, v59, -v59, vcc
	v_fma_f32 v58, v59, v59, 1.0
	v_rsq_f32_e32 v61, v58
	s_nop 0
	v_mul_f32_e32 v62, v61, v59
	v_mul_f32_e32 v55, v62, v53
	v_mul_f32_e32 v56, v62, v52
	v_fma_f32 v52, v61, v52, -v55
	v_fma_f32 v53, v61, v53, v56
	v_mul_f32_e32 v55, v52, v52
	v_mul_f32_e32 v56, v54, v54
	v_mul_f32_e32 v57, v52, v54
	v_add_f32_dpp v55, v55, v55 quad_perm:[1,0,3,2] row_mask:0xf bank_mask:0xf
	v_add_f32_dpp v56, v56, v56 quad_perm:[1,0,3,2] row_mask:0xf bank_mask:0xf
	v_add_f32_dpp v57, v57, v57 quad_perm:[1,0,3,2] row_mask:0xf bank_mask:0xf
	v_add_f32_dpp v55, v55, v55 quad_perm:[2,3,0,1] row_mask:0xf bank_mask:0xf
	v_add_f32_dpp v56, v56, v56 quad_perm:[2,3,0,1] row_mask:0xf bank_mask:0xf
	v_add_f32_dpp v57, v57, v57 quad_perm:[2,3,0,1] row_mask:0xf bank_mask:0xf
	v_sub_f32_e32 v60, v56, v55
	v_mul_f32_e32 v58, v57, v57
	v_cmp_gt_f32_e32 vcc, 0, v60
	v_mul_f32_e32 v59, v60, v60
	v_fmac_f32_e32 v59, 4.0, v58
	v_sqrt_f32_e32 v59, v59
	v_mul_f32_e32 v63, v62, v41
	v_mul_f32_e32 v43, v62, v40
	v_fma_f32 v40, v61, v40, -v63
	v_fma_f32 v41, v61, v41, v43
	v_add_f32_e64 v59, |v60|, v59
	v_add_f32_e32 v59, 0x0da24260, v59
	v_rcp_f32_e32 v59, v59
	v_add_f32_e32 v58, v57, v57
	v_mul_f32_e32 v59, v58, v59
	v_cndmask_b32_e64 v59, v59, -v59, vcc
	v_fma_f32 v58, v59, v59, 1.0
	v_rsq_f32_e32 v61, v58
	s_nop 0
	v_mul_f32_e32 v62, v61, v59
	v_mul_f32_e32 v55, v62, v54
	v_mul_f32_e32 v56, v62, v52
	v_fma_f32 v52, v61, v52, -v55
	v_fma_f32 v54, v61, v54, v56
	v_mul_f32_e32 v55, v53, v53
	v_mul_f32_e32 v56, v54, v54
	v_mul_f32_e32 v57, v53, v54
	v_add_f32_dpp v55, v55, v55 quad_perm:[1,0,3,2] row_mask:0xf bank_mask:0xf
	v_add_f32_dpp v56, v56, v56 quad_perm:[1,0,3,2] row_mask:0xf bank_mask:0xf
	v_add_f32_dpp v57, v57, v57 quad_perm:[1,0,3,2] row_mask:0xf bank_mask:0xf
	v_add_f32_dpp v55, v55, v55 quad_perm:[2,3,0,1] row_mask:0xf bank_mask:0xf
	v_add_f32_dpp v56, v56, v56 quad_perm:[2,3,0,1] row_mask:0xf bank_mask:0xf
	v_add_f32_dpp v57, v57, v57 quad_perm:[2,3,0,1] row_mask:0xf bank_mask:0xf
	v_sub_f32_e32 v60, v56, v55
	v_mul_f32_e32 v58, v57, v57
	v_cmp_gt_f32_e32 vcc, 0, v60
	v_mul_f32_e32 v59, v60, v60
	v_fmac_f32_e32 v59, 4.0, v58
	v_sqrt_f32_e32 v59, v59
	v_mul_f32_e32 v63, v62, v42
	v_mul_f32_e32 v43, v62, v40
	v_fma_f32 v40, v61, v40, -v63
	v_fma_f32 v42, v61, v42, v43
	v_add_f32_e64 v59, |v60|, v59
	v_add_f32_e32 v59, 0x0da24260, v59
	v_rcp_f32_e32 v59, v59
	v_add_f32_e32 v58, v57, v57
	v_mul_f32_e32 v59, v58, v59
	v_cndmask_b32_e64 v59, v59, -v59, vcc
	v_fma_f32 v58, v59, v59, 1.0
	v_rsq_f32_e32 v61, v58
	s_nop 0
	v_mul_f32_e32 v62, v61, v59
	v_mul_f32_e32 v55, v62, v54
	v_mul_f32_e32 v56, v62, v53
	v_fma_f32 v53, v61, v53, -v55
	v_fma_f32 v54, v61, v54, v56
	v_mul_f32_e32 v63, v62, v42
	v_mul_f32_e32 v43, v62, v41
	v_fma_f32 v41, v61, v41, -v63
	v_fma_f32 v42, v61, v42, v43
	v_mul_f32_e32 v55, v52, v52
	v_mul_f32_e32 v56, v53, v53
	v_mul_f32_e32 v57, v54, v54
	v_add_f32_dpp v55, v55, v55 quad_perm:[1,0,3,2] row_mask:0xf bank_mask:0xf
	v_add_f32_dpp v56, v56, v56 quad_perm:[1,0,3,2] row_mask:0xf bank_mask:0xf
	v_add_f32_dpp v57, v57, v57 quad_perm:[1,0,3,2] row_mask:0xf bank_mask:0xf
	v_add_f32_dpp v55, v55, v55 quad_perm:[2,3,0,1] row_mask:0xf bank_mask:0xf
	v_add_f32_dpp v56, v56, v56 quad_perm:[2,3,0,1] row_mask:0xf bank_mask:0xf
	v_add_f32_dpp v57, v57, v57 quad_perm:[2,3,0,1] row_mask:0xf bank_mask:0xf
	v_cmp_le_f32_e64 s[28:29], v55, v56
	v_cmp_le_f32_e64 s[30:31], v55, v57
	v_cmp_lt_f32_e32 vcc, v57, v56
	s_and_b64 s[28:29], s[28:29], s[30:31]
	s_andn2_b64 s[30:31], vcc, s[28:29]
	v_cndmask_b32_e64 v44, v52, v53, s[28:29]
	v_cndmask_b32_e64 v45, v54, v53, s[30:31]
	v_cndmask_b32_e64 v46, v40, v41, s[28:29]
	v_cndmask_b32_e64 v47, v42, v41, s[30:31]
	v_mul_f32_e32 v58, v44, v44
	s_nop 1
	v_add_f32_dpp v58, v58, v58 quad_perm:[1,0,3,2] row_mask:0xf bank_mask:0xf
	s_nop 1
	v_add_f32_dpp v58, v58, v58 quad_perm:[2,3,0,1] row_mask:0xf bank_mask:0xf
	v_max_f32_e32 v58, 0x3aa2425, v58
	v_rsq_f32_e32 v58, v58
	s_nop 0
	v_mul_f32_e32 v48, v44, v58
	v_mul_f32_e32 v59, v48, v45
	s_nop 1
	v_add_f32_dpp v59, v59, v59 quad_perm:[1,0,3,2] row_mask:0xf bank_mask:0xf
	s_nop 1
	v_add_f32_dpp v59, v59, v59 quad_perm:[2,3,0,1] row_mask:0xf bank_mask:0xf
	v_fma_f32 v49, -v59, v48, v45
	v_mul_f32_e32 v58, v49, v49
	s_nop 1
	v_add_f32_dpp v58, v58, v58 quad_perm:[1,0,3,2] row_mask:0xf bank_mask:0xf
	s_nop 1
	v_add_f32_dpp v58, v58, v58 quad_perm:[2,3,0,1] row_mask:0xf bank_mask:0xf
	v_max_f32_e32 v58, 0x3aa2425, v58
	v_rsq_f32_e32 v58, v58
	s_nop 0
	v_mul_f32_e32 v50, v49, v58
	v_mov_b32_dpp v43, v47 quad_perm:[2,0,1,3] row_mask:0xf bank_mask:0xf
	v_mov_b32_dpp v63, v47 quad_perm:[1,2,0,3] row_mask:0xf bank_mask:0xf
	v_mov_b32_dpp v62, v50 quad_perm:[2,0,1,3] row_mask:0xf bank_mask:0xf
	v_mov_b32_dpp v61, v50 quad_perm:[1,2,0,3] row_mask:0xf bank_mask:0xf
	v_mul_f32_dpp v60, v46, v43 quad_perm:[1,2,0,3] row_mask:0xf bank_mask:0xf
	v_mul_f32_dpp v51, v48, v62 quad_perm:[1,2,0,3] row_mask:0xf bank_mask:0xf
	s_nop 0
	v_fmac_f32_dpp v60, -v46, v63 quad_perm:[2,0,1,3] row_mask:0xf bank_mask:0xf
	v_fmac_f32_dpp v51, -v48, v61 quad_perm:[2,0,1,3] row_mask:0xf bank_mask:0xf
	v_mul_f32_dpp v52, v46, v48 quad_perm:[0,0,0,0] row_mask:0xf bank_mask:0xf
	v_mul_f32_dpp v53, v46, v48 quad_perm:[1,1,1,1] row_mask:0xf bank_mask:0xf
	v_mul_f32_dpp v54, v46, v48 quad_perm:[2,2,2,2] row_mask:0xf bank_mask:0xf
	v_fmac_f32_dpp v52, v47, v50 quad_perm:[0,0,0,0] row_mask:0xf bank_mask:0xf
	v_fmac_f32_dpp v53, v47, v50 quad_perm:[1,1,1,1] row_mask:0xf bank_mask:0xf
	v_fmac_f32_dpp v54, v47, v50 quad_perm:[2,2,2,2] row_mask:0xf bank_mask:0xf
	v_fmac_f32_dpp v52, v60, v51 quad_perm:[0,0,0,0] row_mask:0xf bank_mask:0xf
	v_fmac_f32_dpp v53, v60, v51 quad_perm:[1,1,1,1] row_mask:0xf bank_mask:0xf
	v_fmac_f32_dpp v54, v60, v51 quad_perm:[2,2,2,2] row_mask:0xf bank_mask:0xf
	v_mov_b32_e32 v55, 0
	v_writelane_b32 v55, s32, 48
	v_writelane_b32 v55, s33, 49
	v_writelane_b32 v55, s34, 50
	v_mul_f32_e32 v55, 0xbc800000, v55
	v_mul_f32_e32 v56, v55, v52
	v_mul_f32_e32 v57, v55, v53
	v_mul_f32_e32 v58, v55, v54
	v_add_f32_dpp v56, v56, v56 quad_perm:[1,0,3,2] row_mask:0xf bank_mask:0xf
	v_add_f32_dpp v57, v57, v57 quad_perm:[1,0,3,2] row_mask:0xf bank_mask:0xf
	v_add_f32_dpp v58, v58, v58 quad_perm:[1,0,3,2] row_mask:0xf bank_mask:0xf
	v_add_f32_dpp v56, v56, v56 quad_perm:[2,3,0,1] row_mask:0xf bank_mask:0xf
	v_add_f32_dpp v57, v57, v57 quad_perm:[2,3,0,1] row_mask:0xf bank_mask:0xf
	v_add_f32_dpp v58, v58, v58 quad_perm:[2,3,0,1] row_mask:0xf bank_mask:0xf
	v_cndmask_b32_e64 v52, v52, v56, s[26:27]
	v_cndmask_b32_e64 v53, v53, v57, s[26:27]
	v_cndmask_b32_e64 v54, v54, v58, s[26:27]
	v_subrev_u32_e32 v59, 48, v0
	v_lshlrev_b32_e32 v59, 4, v59
	s_mov_b64 exec, s[36:37]
	ds_write_b96 v59, v[52:54] offset:24576
	s_mov_b64 exec, -1
	s_waitcnt lgkmcnt(0)
.Lsolved:
	s_barrier
	v_mov_b32_e32 v6, 0x6000
	ds_read_b96 v[32:34], v6
	ds_read_b96 v[36:38], v6 offset:16
	ds_read_b96 v[40:42], v6 offset:32
	ds_read_b96 v[44:46], v6 offset:48
	ds_read2_b32 v[48:49], v3 offset0:0 offset1:1
	ds_read_b32 v56, v3 offset:8
	ds_read2_b32 v[50:51], v3 offset0:192 offset1:193
	ds_read_b32 v57, v3 offset:776
	ds_read2_b32 v[52:53], v4 offset0:0 offset1:1
	ds_read_b32 v58, v4 offset:8
	ds_read2_b32 v[54:55], v4 offset0:192 offset1:193
	ds_read_b32 v59, v4 offset:776
	s_waitcnt lgkmcnt(6)
	v_fma_f32 v60, v48, v32, v44
	v_fma_f32 v61, v48, v33, v45
	v_fma_f32 v62, v48, v34, v46
	v_fmac_f32_e32 v60, v49, v36
	v_fmac_f32_e32 v61, v49, v37
	v_fmac_f32_e32 v62, v49, v38
	v_fmac_f32_e32 v60, v56, v40
	v_fmac_f32_e32 v61, v56, v41
	v_fmac_f32_e32 v62, v56, v42
	ds_write2_b32 v3, v60, v61 offset0:0 offset1:1
	ds_write_b32 v3, v62 offset:8
	s_waitcnt lgkmcnt(6)
	v_fma_f32 v35, v50, v32, v44
	v_fma_f32 v39, v50, v33, v45
	v_fma_f32 v43, v50, v34, v46
	v_fmac_f32_e32 v35, v51, v36
	v_fmac_f32_e32 v39, v51, v37
	v_fmac_f32_e32 v43, v51, v38
	v_fmac_f32_e32 v35, v57, v40
	v_fmac_f32_e32 v39, v57, v41
	v_fmac_f32_e32 v43, v57, v42
	ds_write2_b32 v3, v35, v39 offset0:192 offset1:193
	ds_write_b32 v3, v43 offset:776
	s_waitcnt lgkmcnt(6)
	v_fma_f32 v60, v52, v32, v44
	v_fma_f32 v61, v52, v33, v45
	v_fma_f32 v62, v52, v34, v46
	v_fmac_f32_e32 v60, v53, v36
	v_fmac_f32_e32 v61, v53, v37
	v_fmac_f32_e32 v62, v53, v38
	v_fmac_f32_e32 v60, v58, v40
	v_fmac_f32_e32 v61, v58, v41
	v_fmac_f32_e32 v62, v58, v42
	ds_write2_b32 v4, v60, v61 offset0:0 offset1:1
	ds_write_b32 v4, v62 offset:8
	s_waitcnt lgkmcnt(6)
	v_fma_f32 v35, v54, v32, v44
	v_fma_f32 v39, v54, v33, v45
	v_fma_f32 v43, v54, v34, v46
	v_fmac_f32_e32 v35, v55, v36
	v_fmac_f32_e32 v39, v55, v37
	v_fmac_f32_e32 v43, v55, v38
	v_fmac_f32_e32 v35, v59, v40
	v_fmac_f32_e32 v39, v59, v41
	v_fmac_f32_e32 v43, v59, v42
	ds_write2_b32 v4, v35, v39 offset0:192 offset1:193
	ds_write_b32 v4, v43 offset:776
	ds_read_b128 v[48:51], v2
	ds_read_b128 v[52:55], v2 offset:1024
	ds_read_b128 v[56:59], v2 offset:2048
	s_waitcnt lgkmcnt(2)
	global_store_dwordx4 v1, v[48:51], s[10:11] offset:-2048 sc0 sc1
	s_waitcnt lgkmcnt(1)
	global_store_dwordx4 v1, v[52:55], s[10:11] offset:-1024 sc0 sc1
	s_waitcnt lgkmcnt(0)
	global_store_dwordx4 v1, v[56:59], s[10:11] offset:0 sc0 sc1
	ds_read2_b32 v[48:49], v67 offset0:0 offset1:1
	ds_read_b32 v56, v67 offset:8
	ds_read2_b32 v[50:51], v67 offset0:192 offset1:193
	ds_read_b32 v57, v67 offset:776
	ds_read2_b32 v[52:53], v68 offset0:0 offset1:1
	ds_read_b32 v58, v68 offset:8
	ds_read2_b32 v[54:55], v68 offset0:192 offset1:193
	ds_read_b32 v59, v68 offset:776
	s_waitcnt lgkmcnt(6)
	v_fma_f32 v60, v48, v32, v44
	v_fma_f32 v61, v48, v33, v45
	v_fma_f32 v62, v48, v34, v46
	v_fmac_f32_e32 v60, v49, v36
	v_fmac_f32_e32 v61, v49, v37
	v_fmac_f32_e32 v62, v49, v38
	v_fmac_f32_e32 v60, v56, v40
	v_fmac_f32_e32 v61, v56, v41
	v_fmac_f32_e32 v62, v56, v42
	ds_write2_b32 v67, v60, v61 offset0:0 offset1:1
	ds_write_b32 v67, v62 offset:8
	s_waitcnt lgkmcnt(6)
	v_fma_f32 v35, v50, v32, v44
	v_fma_f32 v39, v50, v33, v45
	v_fma_f32 v43, v50, v34, v46
	v_fmac_f32_e32 v35, v51, v36
	v_fmac_f32_e32 v39, v51, v37
	v_fmac_f32_e32 v43, v51, v38
	v_fmac_f32_e32 v35, v57, v40
	v_fmac_f32_e32 v39, v57, v41
	v_fmac_f32_e32 v43, v57, v42
	ds_write2_b32 v67, v35, v39 offset0:192 offset1:193
	ds_write_b32 v67, v43 offset:776
	s_waitcnt lgkmcnt(6)
	v_fma_f32 v60, v52, v32, v44
	v_fma_f32 v61, v52, v33, v45
	v_fma_f32 v62, v52, v34, v46
	v_fmac_f32_e32 v60, v53, v36
	v_fmac_f32_e32 v61, v53, v37
	v_fmac_f32_e32 v62, v53, v38
	v_fmac_f32_e32 v60, v58, v40
	v_fmac_f32_e32 v61, v58, v41
	v_fmac_f32_e32 v62, v58, v42
	ds_write2_b32 v68, v60, v61 offset0:0 offset1:1
	ds_write_b32 v68, v62 offset:8
	s_waitcnt lgkmcnt(6)
	v_fma_f32 v35, v54, v32, v44
	v_fma_f32 v39, v54, v33, v45
	v_fma_f32 v43, v54, v34, v46
	v_fmac_f32_e32 v35, v55, v36
	v_fmac_f32_e32 v39, v55, v37
	v_fmac_f32_e32 v43, v55, v38
	v_fmac_f32_e32 v35, v59, v40
	v_fmac_f32_e32 v39, v59, v41
	v_fmac_f32_e32 v43, v59, v42
	ds_write2_b32 v68, v35, v39 offset0:192 offset1:193
	ds_write_b32 v68, v43 offset:776
	ds_read_b128 v[48:51], v2 offset:3072
	ds_read_b128 v[52:55], v2 offset:4096
	ds_read_b128 v[56:59], v2 offset:5120
	s_waitcnt lgkmcnt(2)
	global_store_dwordx4 v1, v[48:51], s[10:11] offset:1024 sc0 sc1
	s_waitcnt lgkmcnt(1)
	global_store_dwordx4 v1, v[52:55], s[10:11] offset:2048 sc0 sc1
	s_waitcnt lgkmcnt(0)
	s_and_saveexec_b64 s[16:17], s[14:15]
	global_store_dwordx4 v1, v[56:59], s[10:11] offset:3072 sc0 sc1
	s_mov_b64 exec, s[16:17]
	s_add_u32 s10, s10, s39
	s_addc_u32 s11, s11, 0
	s_sub_u32 s38, s38, 1
	s_cmp_lg_u32 s38, 0
	s_cbranch_scc1 .Lrow_loop
.Lexit:
	s_endpgm

	.amdhsa_kernel _Z11align_fusedPKfS0_PKiPf
		.amdhsa_group_segment_fixed_size 24640
		.amdhsa_private_segment_fixed_size 0
		.amdhsa_kernarg_size 32
		.amdhsa_user_sgpr_count 2
		.amdhsa_user_sgpr_dispatch_ptr 0
		.amdhsa_user_sgpr_queue_ptr 0
		.amdhsa_user_sgpr_kernarg_segment_ptr 1
		.amdhsa_user_sgpr_dispatch_id 0
		.amdhsa_user_sgpr_kernarg_preload_length 0
		.amdhsa_user_sgpr_kernarg_preload_offset 0
		.amdhsa_user_sgpr_private_segment_size 0
		.amdhsa_uses_dynamic_stack 0
		.amdhsa_enable_private_segment 0
		.amdhsa_system_sgpr_workgroup_id_x 1
		.amdhsa_system_sgpr_workgroup_id_y 0
		.amdhsa_system_sgpr_workgroup_id_z 0
		.amdhsa_system_sgpr_workgroup_info 0
		.amdhsa_system_vgpr_workitem_id 0
		.amdhsa_next_free_vgpr 128
		.amdhsa_next_free_sgpr 48
		.amdhsa_accum_offset 128
		.amdhsa_reserve_vcc 1
		.amdhsa_float_round_mode_32 0
		.amdhsa_float_round_mode_16_64 0
		.amdhsa_float_denorm_mode_32 3
		.amdhsa_float_denorm_mode_16_64 3
		.amdhsa_dx10_clamp 1
		.amdhsa_ieee_mode 1
		.amdhsa_fp16_overflow 0
		.amdhsa_tg_split 0
		.amdhsa_exception_fp_ieee_invalid_op 0
		.amdhsa_exception_fp_denorm_src 0
		.amdhsa_exception_fp_ieee_div_zero 0
		.amdhsa_exception_fp_ieee_overflow 0
		.amdhsa_exception_fp_ieee_underflow 0
		.amdhsa_exception_fp_ieee_inexact 0
		.amdhsa_exception_int_div_zero 0
	.end_amdhsa_kernel

.Lfunc_end0:
	.size	_Z11align_fusedPKfS0_PKiPf, .Lfunc_end0-_Z11align_fusedPKfS0_PKiPf
	.set _Z11align_fusedPKfS0_PKiPf.num_vgpr, 128
	.set _Z11align_fusedPKfS0_PKiPf.num_agpr, 0
	.set _Z11align_fusedPKfS0_PKiPf.numbered_sgpr, 48
	.set _Z11align_fusedPKfS0_PKiPf.num_named_barrier, 0
	.set _Z11align_fusedPKfS0_PKiPf.private_seg_size, 0
	.set _Z11align_fusedPKfS0_PKiPf.uses_vcc, 1
	.set _Z11align_fusedPKfS0_PKiPf.uses_flat_scratch, 0
	.set _Z11align_fusedPKfS0_PKiPf.has_dyn_sized_stack, 0
	.set _Z11align_fusedPKfS0_PKiPf.has_recursion, 0
	.set _Z11align_fusedPKfS0_PKiPf.has_indirect_call, 0

amdhsa.kernels:
  - .agpr_count:     0
    .args:
      - .actual_access:  read_only
        .address_space:  global
        .offset:         0
        .size:           8
        .value_kind:     global_buffer
      - .actual_access:  read_only
        .address_space:  global
        .offset:         8
        .size:           8
        .value_kind:     global_buffer
      - .actual_access:  read_only
        .address_space:  global
        .offset:         16
        .size:           8
        .value_kind:     global_buffer
      - .actual_access:  write_only
        .address_space:  global
        .offset:         24
        .size:           8
        .value_kind:     global_buffer
    .group_segment_fixed_size: 24640
    .kernarg_segment_align: 8
    .kernarg_segment_size: 32
    .language:       OpenCL C
    .language_version:
      - 2
      - 0
    .max_flat_workgroup_size: 256
    .name:           _Z11align_fusedPKfS0_PKiPf
    .private_segment_fixed_size: 0
    .sgpr_count:     54
    .sgpr_spill_count: 0
    .symbol:         _Z11align_fusedPKfS0_PKiPf.kd
    .uniform_work_group_size: 1
    .uses_dynamic_stack: false
    .vgpr_count:     128
    .vgpr_spill_count: 0
    .wavefront_size: 64
